# attention task prologue: Q loads after the bias-table loop (no longer waited by it); first K/V LDS write waits only for chunk 0 (vmcnt(6))
# speedup vs baseline: 1.0053x; 1.0053x over previous
; __device__ __forceinline__ void ph_attn(const Frame& F, int j) {
;     ...
;     for (int task = wgs; task < NTASK; task += F.G) {
;         const bool lat = task < NLAT;
;         int b, h, rp4 = 0;
;         if (lat) { b = task >> 8; h = (task >> 5) & 7; rp4 = task & 31; } else { const int t2 = task - NLAT; b = t2 >> 3; h = t2 & 7; }
;         const int w0 = (F.wave & 3) * 16, myr0 = 4 * rp4 + 2 * (F.wave >> 2);
;         const int rlo = min(max(4 * rp4 - 4, 0), 120), rhi = min(max(4 * rp4 + 3 - 4, 0), 120) + 7;
;         const int nloc = lat ? (rhi - rlo + 1) : 0;
;         int qrow[2], r0t[2];
;         bf16x8 qf[2][2];
; #pragma unroll
;         for (int T = 0; T < 2; ++T) { r0t[T] = min(max(myr0 + T - 4, 0), 120);
;             qrow[T] = lat ? (TC + b * SEQ + (myr0 + T) * 64 + w0 + l15) : (b * CTXL + (2 * F.wave + T) * 16 + l15);
;             qf[T][0] = *(const bf16x8*)(P + (size_t)qrow[T] * 4096 + h * 64 + g * 8);
;             qf[T][1] = *(const bf16x8*)(P + (size_t)qrow[T] * 4096 + h * 64 + 32 + g * 8); }
;         if (lat) for (int i = F.tid; i < 480; i += 512) { const int rr = i >> 5, cc = i & 31; rp_l[i] = (cc < 31) ? rpb[h * 465 + rr * 31 + cc] * 1.4426950408889634f : -1e30f; }
.LBB0_484:
	s_and_b32 s11, s5, 7
	v_readlane_b32 s5, v251, 12
	s_add_i32 s10, s2, s5
	s_lshl_b32 s5, s11, 7
	s_add_u32 s6, s82, s5
	s_addc_u32 s7, s83, 0
	s_lshl_b32 s9, s4, 8
	s_lshl_b32 s26, s4, 13
	v_readlane_b32 s4, v253, 10
	v_readlane_b32 s5, v251, 32
	s_or_b32 s17, s26, s4
	s_lshl_b32 s4, s10, 6
	s_add_i32 s13, s9, s5
	s_add_i32 s16, s4, s17
	s_and_b64 s[4:5], s[46:47], exec
	s_cselect_b32 s4, s16, s13
	s_or_b32 s16, s10, 1
	v_or_b32_e32 v126, s4, v158
	s_lshl_b32 s4, s16, 6
	s_add_i32 s17, s4, s17
	s_or_b32 s13, s13, 16
	v_ashrrev_i32_e32 v127, 31, v126
	s_and_b64 s[4:5], s[46:47], exec
	s_cselect_b32 s4, s17, s13
	v_or_b32_e32 v124, s4, v158
	v_ashrrev_i32_e32 v125, 31, v124
	s_and_saveexec_b64 s[4:5], s[0:1]
	s_cbranch_execz .LBB0_489
	s_mul_i32 s0, s11, 0x1d1
	v_add_u32_e32 v0, s0, v195
	s_mov_b64 s[0:1], 0
	v_mov_b32_e32 v1, v197
	v_mov_b32_e32 v3, v145
	s_branch .LBB0_487

; __device__ __forceinline__ void ph_attn(const Frame& F, int j) {
;     ...
;         const int rlo = min(max(4 * rp4 - 4, 0), 120), rhi = min(max(4 * rp4 + 3 - 4, 0), 120) + 7;
;         const int nloc = lat ? (rhi - rlo + 1) : 0;
;         int qrow[2], r0t[2];
;         bf16x8 qf[2][2];
; #pragma unroll
;         for (int T = 0; T < 2; ++T) { r0t[T] = min(max(myr0 + T - 4, 0), 120);
;             qrow[T] = lat ? (TC + b * SEQ + (myr0 + T) * 64 + w0 + l15) : (b * CTXL + (2 * F.wave + T) * 16 + l15);
;             qf[T][0] = *(const bf16x8*)(P + (size_t)qrow[T] * 4096 + h * 64 + g * 8);
;             qf[T][1] = *(const bf16x8*)(P + (size_t)qrow[T] * 4096 + h * 64 + 32 + g * 8); }
;         if (lat) for (int i = F.tid; i < 480; i += 512) { const int rr = i >> 5, cc = i & 31; rp_l[i] = (cc < 31) ? rpb[h * 465 + rr * 31 + cc] * 1.4426950408889634f : -1e30f; }
;         f32x4 oacc[2][4];
; #pragma unroll
;         for (int T = 0; T < 2; ++T)
; #pragma unroll
;             for (int dt = 0; dt < 4; ++dt) oacc[T][dt] = (f32x4){0.f, 0.f, 0.f, 0.f};
;         float mrun[2] = {-1e30f, -1e30f}, lrun[2] = {0.f, 0.f};
;         const int nch = nloc + 4;
.LBB0_489:
	s_or_b64 exec, exec, s[4:5]
	s_lshl_b32 s4, s11, 7
	s_add_u32 s6, s82, s4
	s_addc_u32 s7, s83, 0
	v_lshlrev_b64 v[0:1], 13, v[126:127]
	v_lshl_add_u64 v[0:1], s[6:7], 0, v[0:1]
	v_lshl_add_u64 v[0:1], v[0:1], 0, v[118:119]
	global_load_dwordx4 v[4:7], v[0:1], off
	global_load_dwordx4 v[8:11], v[0:1], off offset:64
	v_lshlrev_b64 v[0:1], 13, v[124:125]
	v_lshl_add_u64 v[0:1], s[6:7], 0, v[0:1]
	v_lshl_add_u64 v[0:1], v[0:1], 0, v[118:119]
	global_load_dwordx4 v[12:15], v[0:1], off
	global_load_dwordx4 v[16:19], v[0:1], off offset:64
	v_sub_u32_e64 v0, s2, 1 clamp
	s_lshl_b32 s4, s11, 6
	s_max_u32 s11, s2, 4
	v_min_u32_e32 v0, 0x78, v0
	v_subrev_u32_e32 v0, s11, v0
	v_add_u32_e32 v0, 12, v0
	v_cndmask_b32_e64 v214, 0, v0, s[46:47]
	v_sub_u32_e64 v0, s2, 4 clamp
	v_cmp_gt_i32_e32 vcc, 1, v214
	v_readfirstlane_b32 s13, v0
	v_add_u32_e32 v215, 3, v214
	s_cbranch_vccz .LBB0_491
	v_min_i32_e32 v0, 0, v215
	v_sub_u32_e32 v0, v0, v214
	v_lshlrev_b32_e32 v0, 6, v0
	v_add_u32_e32 v0, s9, v0
	s_cbranch_execz .LBB0_492
	s_branch .LBB0_493

; __device__ __forceinline__ void lds_barrier() { asm volatile("s_waitcnt lgkmcnt(0)\n\ts_barrier" ::: "memory"); }
; #define ATT_WRITE(buf_, kq_, vq_) do { const int key = F.tid >> 3, ds = (F.tid & 7) * 8; LAS bf16_t* Kd = Ks0 + (buf_) * 9216; LAS bf16_t* Vd = Kd + 4608; \
;             *(LAS u32x4*)(Kd + key * 72 + ds) = kq_; *(LAS u32x4*)(Vd + key * 72 + ds) = vq_; } while (0)
; __device__ __forceinline__ void ph_attn(const Frame& F, int j) {
;     ...
;         f32x4 oacc[2][4];
; #pragma unroll
;         for (int T = 0; T < 2; ++T)
; #pragma unroll
;             for (int dt = 0; dt < 4; ++dt) oacc[T][dt] = (f32x4){0.f, 0.f, 0.f, 0.f};
;         float mrun[2] = {-1e30f, -1e30f}, lrun[2] = {0.f, 0.f};
;         const int nch = nloc + 4;
;     ...
;         ATT_LOAD(k0, v0, 0); ATT_LOAD(k1, v1, 1); ATT_LOAD(k2, v2, 2); ATT_LOAD(k3, v3, 3);
;         lds_barrier();
;         ATT_WRITE(0, k0, v0);
;         lds_barrier();
.LBB0_505:
	v_add_u32_e32 v0, v1, v194
	v_ashrrev_i32_e32 v1, 31, v0
	v_lshlrev_b64 v[0:1], 13, v[0:1]
	v_lshl_add_u64 v[0:1], s[82:83], 0, v[0:1]
	v_lshl_add_u64 v[0:1], v[0:1], 0, s[64:65]
	v_mov_b32_e32 v121, v2
	v_lshl_add_u64 v[0:1], v[0:1], 0, v[120:121]
	global_load_dwordx4 v[36:39], v[0:1], off offset:1024
	global_load_dwordx4 v[40:43], v[0:1], off offset:2048
	s_waitcnt lgkmcnt(0)
	s_barrier
	s_waitcnt vmcnt(6)
	ds_write_b128 v196, v[44:47]
	ds_write_b128 v196, v[48:51] offset:9216
	s_waitcnt lgkmcnt(0)
	s_barrier
	v_cmp_gt_i32_e32 vcc, -3, v214
	s_cbranch_vccnz .LBB0_477
	s_max_i32 s0, s10, 4
	s_add_i32 s0, s0, -4
	s_min_u32 s24, s0, 0x78
	s_max_i32 s0, s16, 4
	s_add_i32 s0, s0, -4
	s_min_u32 s25, s0, 0x78
	s_lshl_b32 s0, s11, 5
	v_readlane_b32 s1, v253, 33
	s_add_i32 s0, s1, s0
	s_lshl_b32 s1, s2, 5
	s_sub_i32 s29, s0, s1
	s_lshl_b32 s0, s11, 7
	s_lshl_b32 s1, s2, 7
	v_mov_b32_e32 v64, v2
	v_mov_b32_e32 v65, v2
	v_mov_b32_e32 v66, v2
	v_mov_b32_e32 v67, v2
	s_sub_i32 s0, s0, s1
	v_readlane_b32 s1, v253, 34
	v_mov_b32_e32 v3, v2
	v_mov_b64_e32 v[60:61], v[64:65]
	v_mov_b64_e32 v[56:57], v[64:65]
	v_mov_b64_e32 v[52:53], v[64:65]
	v_mov_b64_e32 v[102:103], v[66:67]
	v_mov_b64_e32 v[86:87], v[66:67]
	v_mov_b64_e32 v[82:83], v[66:67]
	v_mov_b64_e32 v[74:75], v[66:67]
	v_add_u32_e32 v121, 4, v214
	s_bitset1_b32 s26, 10
	v_sub_u32_e32 v216, 0, v214
	s_add_i32 s27, s24, 8
	s_add_i32 s28, s25, 8
	v_lshl_add_u64 v[0:1], v[116:117], 0, s[64:65]
	s_mov_b32 s30, 7
	s_add_i32 s31, s1, s0
	v_mov_b32_e32 v218, 0xf149f2ca
	v_mov_b64_e32 v[62:63], v[66:67]
	v_mov_b64_e32 v[58:59], v[66:67]
	v_mov_b64_e32 v[54:55], v[66:67]
	v_mov_b64_e32 v[100:101], v[64:65]
	v_mov_b64_e32 v[84:85], v[64:65]
	v_mov_b64_e32 v[80:81], v[64:65]
	v_mov_b64_e32 v[72:73], v[64:65]
	v_mov_b32_e32 v217, 0xf149f2ca
	v_mov_b64_e32 v[128:129], v[2:3]
	s_branch .LBB0_509
